# E31: E25 + MFMA/VALU interleave (lever 8) in the NSA sel-far loop: the softmax row-sum adds and l-update fma are deferred into the PV MFMA gaps (one VALU per gap, same operation order, bit-identical)
# speedup vs baseline: 1.0008x; 1.0008x over previous
.LBB0_697:
	v_sub_f32_e32 v0, v5, v134
	v_fmamk_f32 v5, v98, 0x3fb8aa3b, v0
	v_exp_f32_e32 v98, v5
	v_fmamk_f32 v5, v99, 0x3fb8aa3b, v0
	v_exp_f32_e32 v99, v5
	v_fmamk_f32 v5, v100, 0x3fb8aa3b, v0
	v_exp_f32_e32 v100, v5
	v_fmamk_f32 v5, v101, 0x3fb8aa3b, v0
	v_exp_f32_e32 v101, v5
	v_fmamk_f32 v94, v94, 0x3fb8aa3b, v0
	v_exp_f32_e32 v94, v94
	v_fmamk_f32 v95, v95, 0x3fb8aa3b, v0
	v_exp_f32_e32 v95, v95
	v_fmamk_f32 v96, v96, 0x3fb8aa3b, v0
	v_exp_f32_e32 v96, v96
	v_fmamk_f32 v97, v97, 0x3fb8aa3b, v0
	v_exp_f32_e32 v97, v97
	v_fmamk_f32 v90, v90, 0x3fb8aa3b, v0
	v_exp_f32_e32 v90, v90
	v_fmamk_f32 v91, v91, 0x3fb8aa3b, v0
	v_exp_f32_e32 v91, v91
	v_fmamk_f32 v92, v92, 0x3fb8aa3b, v0
	v_exp_f32_e32 v92, v92
	v_fmamk_f32 v93, v93, 0x3fb8aa3b, v0
	v_exp_f32_e32 v93, v93
	v_fmamk_f32 v86, v86, 0x3fb8aa3b, v0
	v_exp_f32_e32 v198, v86
	v_fmamk_f32 v86, v87, 0x3fb8aa3b, v0
	v_exp_f32_e32 v199, v86
	v_fmamk_f32 v86, v88, 0x3fb8aa3b, v0
	v_exp_f32_e32 v200, v86
	v_fmac_f32_e32 v0, 0x3fb8aa3b, v89
	v_exp_f32_e32 v0, v0
	v_mov_b32_e32 v248, v136
	v_mov_b32_e32 v249, v4
	v_sub_f32_e32 v4, v137, v125
	v_fmamk_f32 v82, v82, 0x3fb8aa3b, v4
	v_exp_f32_e32 v82, v82
	v_fmamk_f32 v83, v83, 0x3fb8aa3b, v4
	v_exp_f32_e32 v83, v83
	v_fmamk_f32 v84, v84, 0x3fb8aa3b, v4
	v_exp_f32_e32 v84, v84
	v_fmamk_f32 v85, v85, 0x3fb8aa3b, v4
	v_exp_f32_e32 v85, v85
	v_fmamk_f32 v78, v78, 0x3fb8aa3b, v4
	v_add_f32_e32 v86, 0, v82
	v_exp_f32_e32 v87, v78
	v_fmamk_f32 v78, v79, 0x3fb8aa3b, v4
	v_add_f32_e32 v86, v83, v86
	v_exp_f32_e32 v88, v78
	v_fmamk_f32 v78, v80, 0x3fb8aa3b, v4
	v_add_f32_e32 v86, v84, v86
	v_exp_f32_e32 v89, v78
	v_fmamk_f32 v78, v81, 0x3fb8aa3b, v4
	v_add_f32_e32 v86, v85, v86
	v_exp_f32_e32 v81, v78
	v_fmamk_f32 v74, v74, 0x3fb8aa3b, v4
	v_add_f32_e32 v78, v87, v86
	v_exp_f32_e32 v136, v74
	v_fmamk_f32 v74, v75, 0x3fb8aa3b, v4
	v_add_f32_e32 v78, v88, v78
	v_exp_f32_e32 v137, v74
	v_fmamk_f32 v74, v76, 0x3fb8aa3b, v4
	v_add_f32_e32 v78, v89, v78
	v_exp_f32_e32 v201, v74
	v_fmamk_f32 v74, v77, 0x3fb8aa3b, v4
	v_add_f32_e32 v250, v81, v78
	v_exp_f32_e32 v202, v74
	v_fmamk_f32 v70, v70, 0x3fb8aa3b, v4
	v_exp_f32_e32 v203, v70
	v_fmamk_f32 v70, v71, 0x3fb8aa3b, v4
	v_exp_f32_e32 v204, v70
	v_fmamk_f32 v70, v72, 0x3fb8aa3b, v4
	v_exp_f32_e32 v205, v70
	v_fmac_f32_e32 v4, 0x3fb8aa3b, v73
	v_exp_f32_e32 v4, v4
	s_cmp_eq_u32 s83, 0
	s_cselect_b32 s0, 0x8000, s79
	s_add_i32 s0, s0, 0
	v_mov_b32_e32 v251, v2
	v_add_u32_e32 v2, s0, v142
	ds_read_b128 v[70:73], v2
	ds_read_b128 v[74:77], v2 offset:2048
	v_cvt_pk_bf16_f32 v78, v82, v83
	v_cvt_pk_bf16_f32 v79, v84, v85
	ds_read_b128 v[82:85], v2 offset:4096
	v_cvt_pk_bf16_f32 v80, v87, v88
	v_cvt_pk_bf16_f32 v81, v89, v81
	v_cvt_pk_bf16_f32 v86, v98, v99
	v_cvt_pk_bf16_f32 v87, v100, v101
	v_cvt_pk_bf16_f32 v88, v94, v95
	v_cvt_pk_bf16_f32 v89, v96, v97
	s_waitcnt lgkmcnt(2)
	v_mfma_f32_16x16x32_bf16 v[66:69], v[70:73], v[78:81], v[66:69]
	v_add_f32_e32 v5, 0, v98
	v_mfma_f32_16x16x32_bf16 v[34:37], v[70:73], v[86:89], v[34:37]
	v_add_f32_e32 v5, v99, v5
	ds_read_b128 v[70:73], v2 offset:6144
	s_waitcnt lgkmcnt(2)
	v_mfma_f32_16x16x32_bf16 v[62:65], v[74:77], v[78:81], v[62:65]
	v_add_f32_e32 v5, v100, v5
	v_mfma_f32_16x16x32_bf16 v[30:33], v[74:77], v[86:89], v[30:33]
	v_add_f32_e32 v5, v101, v5
	ds_read_b128 v[74:77], v2 offset:8192
	s_waitcnt lgkmcnt(2)
	v_mfma_f32_16x16x32_bf16 v[58:61], v[82:85], v[78:81], v[58:61]
	v_add_f32_e32 v5, v94, v5
	v_mfma_f32_16x16x32_bf16 v[26:29], v[82:85], v[86:89], v[26:29]
	v_add_f32_e32 v5, v95, v5
	ds_read_b128 v[82:85], v2 offset:10240
	s_waitcnt lgkmcnt(2)
	v_mfma_f32_16x16x32_bf16 v[54:57], v[70:73], v[78:81], v[54:57]
	v_add_f32_e32 v5, v96, v5
	v_mfma_f32_16x16x32_bf16 v[22:25], v[70:73], v[86:89], v[22:25]
	v_add_f32_e32 v5, v97, v5
	ds_read_b128 v[70:73], v2 offset:12288
	s_waitcnt lgkmcnt(2)
	v_mfma_f32_16x16x32_bf16 v[50:53], v[74:77], v[78:81], v[50:53]
	v_add_f32_e32 v5, v90, v5
	v_mfma_f32_16x16x32_bf16 v[18:21], v[74:77], v[86:89], v[18:21]
	v_add_f32_e32 v5, v91, v5
	ds_read_b128 v[74:77], v2 offset:14336
	v_add_u32_e32 v2, s0, v146
	s_waitcnt lgkmcnt(2)
	v_mfma_f32_16x16x32_bf16 v[46:49], v[82:85], v[78:81], v[46:49]
	v_add_f32_e32 v5, v92, v5
	v_mfma_f32_16x16x32_bf16 v[14:17], v[82:85], v[86:89], v[14:17]
	v_add_f32_e32 v5, v93, v5
	ds_read_b128 v[82:85], v2
	s_waitcnt lgkmcnt(2)
	v_mfma_f32_16x16x32_bf16 v[42:45], v[70:73], v[78:81], v[42:45]
	v_add_f32_e32 v5, v198, v5
	v_mfma_f32_16x16x32_bf16 v[10:13], v[70:73], v[86:89], v[10:13]
	v_add_f32_e32 v5, v199, v5
	ds_read_b128 v[70:73], v2 offset:2048
	s_waitcnt lgkmcnt(2)
	v_mfma_f32_16x16x32_bf16 v[38:41], v[74:77], v[78:81], v[38:41]
	v_add_f32_e32 v5, v200, v5
	v_cvt_pk_bf16_f32 v78, v90, v91
	v_cvt_pk_bf16_f32 v79, v92, v93
	v_cvt_pk_bf16_f32 v80, v198, v199
	v_mfma_f32_16x16x32_bf16 v[6:9], v[74:77], v[86:89], v[6:9]
	v_add_f32_e32 v5, v0, v5
	ds_read_b128 v[86:89], v2 offset:4096
	v_cvt_pk_bf16_f32 v74, v136, v137
	v_cvt_pk_bf16_f32 v75, v201, v202
	v_cvt_pk_bf16_f32 v76, v203, v204
	v_cvt_pk_bf16_f32 v77, v205, v4
	v_cvt_pk_bf16_f32 v81, v200, v0
	s_nop 0
	s_waitcnt lgkmcnt(2)
	v_mfma_f32_16x16x32_bf16 v[66:69], v[82:85], v[74:77], v[66:69]
	v_fmac_f32_e32 v5, v248, v249
	v_mfma_f32_16x16x32_bf16 v[34:37], v[82:85], v[78:81], v[34:37]
	v_add_f32_e32 v250, v136, v250
	ds_read_b128 v[82:85], v2 offset:6144
	s_waitcnt lgkmcnt(2)
	v_mfma_f32_16x16x32_bf16 v[62:65], v[70:73], v[74:77], v[62:65]
	v_add_f32_e32 v250, v137, v250
	v_mfma_f32_16x16x32_bf16 v[30:33], v[70:73], v[78:81], v[30:33]
	v_add_f32_e32 v250, v201, v250
	ds_read_b128 v[70:73], v2 offset:8192
	s_waitcnt lgkmcnt(2)
	v_mfma_f32_16x16x32_bf16 v[58:61], v[86:89], v[74:77], v[58:61]
	v_add_f32_e32 v250, v202, v250
	v_mfma_f32_16x16x32_bf16 v[26:29], v[86:89], v[78:81], v[26:29]
	v_add_f32_e32 v250, v203, v250
	ds_read_b128 v[86:89], v2 offset:10240
	s_waitcnt lgkmcnt(2)
	v_mfma_f32_16x16x32_bf16 v[54:57], v[82:85], v[74:77], v[54:57]
	v_add_f32_e32 v250, v204, v250
	v_mfma_f32_16x16x32_bf16 v[22:25], v[82:85], v[78:81], v[22:25]
	v_add_f32_e32 v250, v205, v250
	ds_read_b128 v[82:85], v2 offset:12288
	s_waitcnt lgkmcnt(2)
	v_mfma_f32_16x16x32_bf16 v[50:53], v[70:73], v[74:77], v[50:53]
	v_add_f32_e32 v133, v4, v250
	v_mfma_f32_16x16x32_bf16 v[18:21], v[70:73], v[78:81], v[18:21]
	v_fmac_f32_e32 v133, v135, v251
	ds_read_b128 v[70:73], v2 offset:14336
	s_waitcnt lgkmcnt(2)
	v_mfma_f32_16x16x32_bf16 v[46:49], v[86:89], v[74:77], v[46:49]
	v_mfma_f32_16x16x32_bf16 v[14:17], v[86:89], v[78:81], v[14:17]
	s_waitcnt lgkmcnt(1)
	v_mfma_f32_16x16x32_bf16 v[42:45], v[82:85], v[74:77], v[42:45]
	v_mfma_f32_16x16x32_bf16 v[10:13], v[82:85], v[78:81], v[10:13]
	s_waitcnt lgkmcnt(0)
	v_mfma_f32_16x16x32_bf16 v[38:41], v[70:73], v[74:77], v[38:41]
	s_waitcnt vmcnt(0)
	s_add_i32 s33, s33, 1
	s_add_i32 s0, s8, s33
	v_mfma_f32_16x16x32_bf16 v[6:9], v[70:73], v[78:81], v[6:9]
	s_cmp_eq_u32 s0, 1
	s_cbranch_scc1 .Lx687_exit
	v_mov_b32_e32 v136, v5
	v_mov_b32_e32 v135, v133
	v_mov_b32_e32 v133, v125
	v_mov_b32_e32 v4, v134
	s_add_i32 s0, s33, -1
	s_and_b32 s83, s0, 1
	s_add_i32 s3, s3, 1
	s_lshl_b32 s0, s83, 14
	s_add_i32 s0, s0, 0
	v_add_u32_e32 v0, s0, v140
	s_add_i32 s1, s37, s33
	s_add_i32 s1, s1, -1
	s_mov_b32 s32, 0
	s_add_i32 s98, s33, -1
	s_cmp_ge_u32 s98, s86
	s_cbranch_scc1 .Lx687_pd
	s_cmp_ge_i32 s33, s42
	s_mov_b64 s[98:99], -1
	s_cbranch_scc0 .Lx687_a
	s_add_i32 s98, s8, s33
	s_cmp_ge_i32 s98, s43
	s_cselect_b32 s99, s82, 0
	s_add_i32 s22, s98, s99
	s_mov_b64 s[98:99], 0

.LBB0_700:
	s_lshl_b32 s8, s36, 19
	s_cmp_gt_i32 s82, s86
	s_cbranch_scc1 .LBB0_781
	s_sub_i32 s36, s2, s43
	s_sub_i32 s84, 0, s42
	s_cmp_ge_i32 s82, s42
	s_mov_b64 s[0:1], -1
	s_cbranch_scc0 .LBB0_704
	s_branch .LBB0_703
	s_nop 0
	s_nop 0
	s_nop 0
	s_nop 0
	s_nop 0
	s_nop 0
	s_nop 0
	s_nop 0
	s_nop 0
	s_nop 0
	s_nop 0
	s_nop 0
	s_nop 0
	s_nop 0
	s_nop 0
	s_nop 0
	s_nop 0
	s_nop 0
	s_nop 0
	s_nop 0
	s_nop 0
	s_nop 0
	s_nop 0
	s_nop 0
	s_nop 0
	s_nop 0
	s_nop 0
	s_nop 0
	s_nop 0
	s_nop 0
	s_nop 0
	s_nop 0
	s_nop 0
	s_nop 0
	s_nop 0
	s_nop 0
	s_nop 0
	s_nop 0
	s_nop 0
	s_nop 0
	s_nop 0
	s_nop 0
	s_nop 0
	s_nop 0
	s_nop 0
	s_nop 0
	s_nop 0
